# seam-hosted conversion: waves 1-7 of every workgroup convert expert-weight items while the leader runs the grid barrier after the in-projection GEMM (2 items) and after the first mixer pass (1 item);
# speedup vs baseline: 1.0036x; 1.0036x over previous
.LBB0_36:
	s_barrier
	s_mul_i32 s0, s38, 0xffffff8b
	s_add_i32 s0, s0, 0xd800
	s_cmp_gt_i32 s38, 64
	s_cselect_b32 s2, s0, 0xc000
	s_abs_i32 s0, s34
	v_cvt_f32_u32_e32 v1, s0
	s_sub_i32 s3, 0, s0
	s_add_i32 s1, s36, s34
	v_rcp_iflag_f32_e32 v1, v1
	s_nop 0
	v_mul_f32_e32 v1, 0x4f7ffffe, v1
	v_cvt_u32_f32_e32 v1, v1
	s_nop 0
	v_readfirstlane_b32 s4, v1
	s_mul_i32 s3, s3, s4
	s_mul_hi_u32 s3, s4, s3
	s_add_i32 s3, s4, s3
	s_mul_hi_u32 s4, s3, 0x690
	s_mul_i32 s4, s4, s0
	s_sub_i32 s4, 0x690, s4
	s_sub_i32 s5, s4, s0
	s_cmp_ge_u32 s4, s0
	s_cselect_b32 s4, s5, s4
	s_sub_i32 s5, s4, s0
	s_cmp_ge_u32 s4, s0
	s_cselect_b32 s4, s5, s4
	s_sub_i32 s1, s1, s4
	s_ashr_i32 s26, s1, 31
	s_abs_i32 s1, s1
	s_mul_hi_u32 s4, s1, s3
	s_mul_i32 s4, s4, s0
	s_sub_i32 s1, s1, s4
	s_sub_i32 s4, s1, s0
	s_cmp_ge_u32 s1, s0
	s_cselect_b32 s1, s4, s1
	s_sub_i32 s4, s1, s0
	s_cmp_ge_u32 s1, s0
	s_cselect_b32 s1, s4, s1
	s_xor_b32 s27, s1, s26
	s_sub_i32 s1, s27, s26
	s_cmp_gt_i32 s2, s1
	s_cbranch_scc0 .LBB0_38
	s_add_i32 s2, s34, s2
	s_not_b32 s5, s1
	s_add_i32 s5, s5, s2
	s_ashr_i32 s4, s34, 31
	s_ashr_i32 s2, s5, 31
	s_xor_b32 s2, s2, s4
	s_abs_i32 s4, s5
	s_mul_hi_u32 s3, s4, s3
	s_mul_i32 s5, s3, s0
	s_sub_i32 s4, s4, s5
	s_add_i32 s5, s3, 1
	s_sub_i32 s8, s4, s0
	s_cmp_ge_u32 s4, s0
	s_cselect_b32 s3, s5, s3
	s_cselect_b32 s4, s8, s4
	s_add_i32 s5, s3, 1
	s_cmp_ge_u32 s4, s0
	s_cselect_b32 s0, s5, s3
	s_xor_b32 s0, s0, s2
	s_sub_i32 s35, s0, s2

.LBB0_214:
	s_waitcnt vmcnt(0)
	s_waitcnt vmcnt(0)
	s_barrier
	s_cmp_lt_u32 s80, 64
	s_cbranch_scc1 .Lh1_skip
	s_cmp_lt_i32 s38, 65
	s_cbranch_scc1 .Lh1_skip
	v_writelane_b32 v255, s0, 0
	v_writelane_b32 v255, s1, 1
	v_writelane_b32 v255, s2, 2
	v_writelane_b32 v255, s3, 3
	v_writelane_b32 v255, s4, 4
	v_writelane_b32 v255, s5, 5
	v_writelane_b32 v255, s7, 6
	v_writelane_b32 v255, s8, 7
	v_writelane_b32 v255, s9, 8
	v_writelane_b32 v255, s10, 9
	v_writelane_b32 v255, s11, 10
	v_writelane_b32 v255, s12, 11
	v_writelane_b32 v255, s13, 12
	v_writelane_b32 v255, s14, 13
	v_writelane_b32 v255, s15, 14
	v_writelane_b32 v255, s22, 15
	v_writelane_b32 v255, s23, 16
	v_writelane_b32 v255, s24, 17
	v_writelane_b32 v255, s25, 18
	v_writelane_b32 v255, s26, 19
	v_writelane_b32 v255, s27, 20
	v_writelane_b32 v255, s28, 21
	v_writelane_b32 v255, s29, 22
	v_writelane_b32 v255, s30, 23
	v_writelane_b32 v255, s31, 24
	v_writelane_b32 v255, s33, 25
	v_writelane_b32 v255, s34, 26
	v_writelane_b32 v255, s35, 27
	v_writelane_b32 v255, s37, 28
	v_writelane_b32 v255, s39, 29
	v_writelane_b32 v255, s40, 30
	v_writelane_b32 v255, s41, 31
	v_writelane_b32 v255, s42, 32
	v_writelane_b32 v255, s43, 33
	v_writelane_b32 v255, s44, 34
	v_mov_b32_e32 v110, v0
	v_mov_b32_e32 v111, v1
	v_mov_b32_e32 v112, v2
	v_mov_b32_e32 v113, v3
	v_mov_b32_e32 v114, v4
	v_mov_b32_e32 v115, v5
	v_mov_b32_e32 v116, v6
	v_mov_b32_e32 v117, v7
	v_mov_b32_e32 v118, v8
	v_mov_b32_e32 v119, v9
	v_mov_b32_e32 v120, v10
	v_mov_b32_e32 v121, v11
	v_mov_b32_e32 v122, v12
	v_mov_b32_e32 v123, v13
	v_mov_b32_e32 v124, v14
	v_mov_b32_e32 v125, v15
	v_mov_b32_e32 v126, v16
	v_mov_b32_e32 v127, v17
	v_mov_b32_e32 v128, v18
	v_mov_b32_e32 v129, v19
	v_mov_b32_e32 v130, v20
	v_mov_b32_e32 v131, v21
	v_mov_b32_e32 v132, v22
	v_mov_b32_e32 v133, v23
	v_mov_b32_e32 v134, v24
	v_mov_b32_e32 v135, v25
	v_mov_b32_e32 v136, v26
	v_mov_b32_e32 v137, v27
	v_mov_b32_e32 v138, v28
	v_mov_b32_e32 v139, v29
	v_mov_b32_e32 v140, v30
	v_mov_b32_e32 v141, v31
	v_mov_b32_e32 v142, v32
	v_mov_b32_e32 v143, v33
	v_mov_b32_e32 v144, v34
	v_mov_b32_e32 v145, v35
	v_mov_b32_e32 v146, v36
	v_mov_b32_e32 v147, v37
	v_mov_b32_e32 v148, v38
	v_mov_b32_e32 v149, v39
	v_mov_b32_e32 v150, v40
	v_mov_b32_e32 v151, v41
	v_mov_b32_e32 v152, v42
	v_mov_b32_e32 v153, v43
	v_mov_b32_e32 v154, v44
	v_mov_b32_e32 v155, v45
	v_mov_b32_e32 v156, v46
	v_mov_b32_e32 v157, v47
	v_mov_b32_e32 v158, v48
	v_mov_b32_e32 v159, v49
	v_mov_b32_e32 v160, v50
	v_mov_b32_e32 v161, v51
	v_mov_b32_e32 v162, v66
	v_mov_b32_e32 v163, v82
	s_mul_i32 s0, s38, 0xffffff8b
	s_add_i32 s0, s0, 0xd800
	s_mul_i32 s1, s6, 7
	s_add_i32 s1, s1, s88
	s_add_i32 s1, s1, s0
	s_add_i32 s1, s1, 0x0
	s_mul_i32 s34, s38, 7
	s_mul_i32 s0, s34, 0
	s_add_i32 s1, s1, s0
	s_add_i32 s1, s1, -1
	s_mov_b32 s26, 0
	s_mov_b32 s27, s1
	s_movk_i32 s35, 2
	s_mul_i32 s7, s88, 0x4200
	s_mov_b64 s[22:23], s[86:87]
	s_mov_b64 s[24:25], s[18:19]
	v_mbcnt_hi_u32_b32 v0, -1, v217
	s_and_b32 s0, s80, 0xffffffc0
	v_add_u32_e32 v82, s0, v0

.Lh1_exit:
	s_waitcnt vmcnt(0) lgkmcnt(0)
	v_mov_b32_e32 v0, v110
	v_mov_b32_e32 v1, v111
	v_mov_b32_e32 v2, v112
	v_mov_b32_e32 v3, v113
	v_mov_b32_e32 v4, v114
	v_mov_b32_e32 v5, v115
	v_mov_b32_e32 v6, v116
	v_mov_b32_e32 v7, v117
	v_mov_b32_e32 v8, v118
	v_mov_b32_e32 v9, v119
	v_mov_b32_e32 v10, v120
	v_mov_b32_e32 v11, v121
	v_mov_b32_e32 v12, v122
	v_mov_b32_e32 v13, v123
	v_mov_b32_e32 v14, v124
	v_mov_b32_e32 v15, v125
	v_mov_b32_e32 v16, v126
	v_mov_b32_e32 v17, v127
	v_mov_b32_e32 v18, v128
	v_mov_b32_e32 v19, v129
	v_mov_b32_e32 v20, v130
	v_mov_b32_e32 v21, v131
	v_mov_b32_e32 v22, v132
	v_mov_b32_e32 v23, v133
	v_mov_b32_e32 v24, v134
	v_mov_b32_e32 v25, v135
	v_mov_b32_e32 v26, v136
	v_mov_b32_e32 v27, v137
	v_mov_b32_e32 v28, v138
	v_mov_b32_e32 v29, v139
	v_mov_b32_e32 v30, v140
	v_mov_b32_e32 v31, v141
	v_mov_b32_e32 v32, v142
	v_mov_b32_e32 v33, v143
	v_mov_b32_e32 v34, v144
	v_mov_b32_e32 v35, v145
	v_mov_b32_e32 v36, v146
	v_mov_b32_e32 v37, v147
	v_mov_b32_e32 v38, v148
	v_mov_b32_e32 v39, v149
	v_mov_b32_e32 v40, v150
	v_mov_b32_e32 v41, v151
	v_mov_b32_e32 v42, v152
	v_mov_b32_e32 v43, v153
	v_mov_b32_e32 v44, v154
	v_mov_b32_e32 v45, v155
	v_mov_b32_e32 v46, v156
	v_mov_b32_e32 v47, v157
	v_mov_b32_e32 v48, v158
	v_mov_b32_e32 v49, v159
	v_mov_b32_e32 v50, v160
	v_mov_b32_e32 v51, v161
	v_mov_b32_e32 v66, v162
	v_mov_b32_e32 v82, v163
	v_readlane_b32 s0, v255, 0
	v_readlane_b32 s1, v255, 1
	v_readlane_b32 s2, v255, 2
	v_readlane_b32 s3, v255, 3
	v_readlane_b32 s4, v255, 4
	v_readlane_b32 s5, v255, 5
	v_readlane_b32 s7, v255, 6
	v_readlane_b32 s8, v255, 7
	v_readlane_b32 s9, v255, 8
	v_readlane_b32 s10, v255, 9
	v_readlane_b32 s11, v255, 10
	v_readlane_b32 s12, v255, 11
	v_readlane_b32 s13, v255, 12
	v_readlane_b32 s14, v255, 13
	v_readlane_b32 s15, v255, 14
	v_readlane_b32 s22, v255, 15
	v_readlane_b32 s23, v255, 16
	v_readlane_b32 s24, v255, 17
	v_readlane_b32 s25, v255, 18
	v_readlane_b32 s26, v255, 19
	v_readlane_b32 s27, v255, 20
	v_readlane_b32 s28, v255, 21
	v_readlane_b32 s29, v255, 22
	v_readlane_b32 s30, v255, 23
	v_readlane_b32 s31, v255, 24
	v_readlane_b32 s33, v255, 25
	v_readlane_b32 s34, v255, 26
	v_readlane_b32 s35, v255, 27
	v_readlane_b32 s37, v255, 28
	v_readlane_b32 s39, v255, 29
	v_readlane_b32 s40, v255, 30
	v_readlane_b32 s41, v255, 31
	v_readlane_b32 s42, v255, 32
	v_readlane_b32 s43, v255, 33
	v_readlane_b32 s44, v255, 34
	s_nop 3
.Lh1_skip:
	s_and_saveexec_b64 s[4:5], s[8:9]
	s_cbranch_execz .LBB0_266
	s_add_i32 s0, 0, 0x24a60
	v_mov_b32_e32 v0, s0
	s_waitcnt vmcnt(0) expcnt(0) lgkmcnt(0)
	ds_read_b32 v2, v0
	s_add_i32 s0, 0, 0x24a64
	v_mov_b32_e32 v0, s0
	ds_read_b32 v0, v0
	s_waitcnt lgkmcnt(1)
	v_cmp_ne_u32_e32 vcc, 0, v2
	s_cbranch_vccnz .LBB0_230
	s_add_u32 s8, s18, 0x4200
	s_addc_u32 s9, s19, 0
	s_add_u32 s10, s18, 0x4400
	s_addc_u32 s11, s19, 0
	s_add_u32 s12, s18, 0x4500
	s_addc_u32 s13, s19, 0
	s_add_u32 s14, s18, 0x4600
	s_addc_u32 s15, s19, 0
	s_add_u32 s20, s18, 0x4700
	s_addc_u32 s21, s19, 0
	s_add_u32 s22, s18, 0x4800
	s_addc_u32 s23, s19, 0
	s_add_u32 s24, s18, 0x4900
	s_addc_u32 s25, s19, 0
	s_add_u32 s26, s18, 0x4a00
	s_addc_u32 s27, s19, 0
	s_add_u32 s28, s18, 0x4b00
	s_addc_u32 s29, s19, 0
	s_add_u32 s30, s18, 0x4c00
	s_addc_u32 s31, s19, 0
	s_add_u32 s48, s18, 0x4d00
	s_addc_u32 s49, s19, 0
	s_add_u32 s50, s18, 0x4e00
	s_addc_u32 s51, s19, 0
	s_add_u32 s52, s18, 0x4f00
	s_addc_u32 s53, s19, 0
	s_add_u32 s54, s18, 0x5000
	s_load_dwordx2 s[0:1], s[96:97], 0x4
	s_addc_u32 s55, s19, 0
	s_add_u32 s56, s18, 0x5100
	s_addc_u32 s57, s19, 0
	s_add_u32 s58, s18, 0x5200
	s_addc_u32 s59, s19, 0
	s_waitcnt lgkmcnt(0)
	s_mul_i32 s0, s0, s38
	s_add_u32 s60, s18, 0x5300
	s_mul_i32 s0, s0, s1
	s_addc_u32 s61, s19, 0
	s_mov_b32 s1, 1
	v_mov_b32_e32 v16, 0
	s_branch .LBB0_218

.LBB0_300:
	s_waitcnt vmcnt(0)
	s_waitcnt vmcnt(0)
	s_barrier
	s_cmp_lt_u32 s80, 64
	s_cbranch_scc1 .Lh2_skip
	s_cmp_lt_i32 s38, 65
	s_cbranch_scc1 .Lh2_skip
	v_writelane_b32 v255, s0, 0
	v_writelane_b32 v255, s1, 1
	v_writelane_b32 v255, s2, 2
	v_writelane_b32 v255, s3, 3
	v_writelane_b32 v255, s4, 4
	v_writelane_b32 v255, s5, 5
	v_writelane_b32 v255, s7, 6
	v_writelane_b32 v255, s8, 7
	v_writelane_b32 v255, s9, 8
	v_writelane_b32 v255, s10, 9
	v_writelane_b32 v255, s11, 10
	v_writelane_b32 v255, s12, 11
	v_writelane_b32 v255, s13, 12
	v_writelane_b32 v255, s14, 13
	v_writelane_b32 v255, s15, 14
	v_writelane_b32 v255, s22, 15
	v_writelane_b32 v255, s23, 16
	v_writelane_b32 v255, s24, 17
	v_writelane_b32 v255, s25, 18
	v_writelane_b32 v255, s26, 19
	v_writelane_b32 v255, s27, 20
	v_writelane_b32 v255, s28, 21
	v_writelane_b32 v255, s29, 22
	v_writelane_b32 v255, s30, 23
	v_writelane_b32 v255, s31, 24
	v_writelane_b32 v255, s33, 25
	v_writelane_b32 v255, s34, 26
	v_writelane_b32 v255, s35, 27
	v_writelane_b32 v255, s37, 28
	v_writelane_b32 v255, s39, 29
	v_writelane_b32 v255, s40, 30
	v_writelane_b32 v255, s41, 31
	v_writelane_b32 v255, s42, 32
	v_writelane_b32 v255, s43, 33
	v_writelane_b32 v255, s44, 34
	v_mov_b32_e32 v110, v0
	v_mov_b32_e32 v111, v1
	v_mov_b32_e32 v112, v2
	v_mov_b32_e32 v113, v3
	v_mov_b32_e32 v114, v4
	v_mov_b32_e32 v115, v5
	v_mov_b32_e32 v116, v6
	v_mov_b32_e32 v117, v7
	v_mov_b32_e32 v118, v8
	v_mov_b32_e32 v119, v9
	v_mov_b32_e32 v120, v10
	v_mov_b32_e32 v121, v11
	v_mov_b32_e32 v122, v12
	v_mov_b32_e32 v123, v13
	v_mov_b32_e32 v124, v14
	v_mov_b32_e32 v125, v15
	v_mov_b32_e32 v126, v16
	v_mov_b32_e32 v127, v17
	v_mov_b32_e32 v128, v18
	v_mov_b32_e32 v129, v19
	v_mov_b32_e32 v130, v20
	v_mov_b32_e32 v131, v21
	v_mov_b32_e32 v132, v22
	v_mov_b32_e32 v133, v23
	v_mov_b32_e32 v134, v24
	v_mov_b32_e32 v135, v25
	v_mov_b32_e32 v136, v26
	v_mov_b32_e32 v137, v27
	v_mov_b32_e32 v138, v28
	v_mov_b32_e32 v139, v29
	v_mov_b32_e32 v140, v30
	v_mov_b32_e32 v141, v31
	v_mov_b32_e32 v142, v32
	v_mov_b32_e32 v143, v33
	v_mov_b32_e32 v144, v34
	v_mov_b32_e32 v145, v35
	v_mov_b32_e32 v146, v36
	v_mov_b32_e32 v147, v37
	v_mov_b32_e32 v148, v38
	v_mov_b32_e32 v149, v39
	v_mov_b32_e32 v150, v40
	v_mov_b32_e32 v151, v41
	v_mov_b32_e32 v152, v42
	v_mov_b32_e32 v153, v43
	v_mov_b32_e32 v154, v44
	v_mov_b32_e32 v155, v45
	v_mov_b32_e32 v156, v46
	v_mov_b32_e32 v157, v47
	v_mov_b32_e32 v158, v48
	v_mov_b32_e32 v159, v49
	v_mov_b32_e32 v160, v50
	v_mov_b32_e32 v161, v51
	v_mov_b32_e32 v162, v66
	v_mov_b32_e32 v163, v82
	s_mul_i32 s0, s38, 0xffffff8b
	s_add_i32 s0, s0, 0xd800
	s_mul_i32 s1, s6, 7
	s_add_i32 s1, s1, s88
	s_add_i32 s1, s1, s0
	s_add_i32 s1, s1, 0x0
	s_mul_i32 s34, s38, 7
	s_mul_i32 s0, s34, 2
	s_add_i32 s1, s1, s0
	s_add_i32 s1, s1, -1
	s_mov_b32 s26, 0
	s_mov_b32 s27, s1
	s_movk_i32 s35, 1
	s_mul_i32 s7, s88, 0x4200
	s_mov_b64 s[22:23], s[86:87]
	s_mov_b64 s[24:25], s[18:19]
	v_mbcnt_hi_u32_b32 v0, -1, v217
	s_and_b32 s0, s80, 0xffffffc0
	v_add_u32_e32 v82, s0, v0

.Lh2_skip:
	s_and_saveexec_b64 s[2:3], s[8:9]
	s_cbranch_execz .LBB0_352
	s_add_i32 s0, 0, 0x24a60
	v_mov_b32_e32 v0, s0
	s_waitcnt vmcnt(0) expcnt(0) lgkmcnt(0)
	ds_read_b32 v2, v0
	s_add_i32 s0, 0, 0x24a64
	v_mov_b32_e32 v0, s0
	ds_read_b32 v0, v0
	s_waitcnt lgkmcnt(1)
	v_cmp_ne_u32_e32 vcc, 0, v2
	s_cbranch_vccnz .LBB0_316
	s_add_u32 s8, s18, 0x4200
	s_addc_u32 s9, s19, 0
	s_add_u32 s10, s18, 0x4400
	s_addc_u32 s11, s19, 0
	s_add_u32 s12, s18, 0x4500
	s_addc_u32 s13, s19, 0
	s_add_u32 s14, s18, 0x4600
	s_addc_u32 s15, s19, 0
	s_add_u32 s20, s18, 0x4700
	s_addc_u32 s21, s19, 0
	s_add_u32 s22, s18, 0x4800
	s_addc_u32 s23, s19, 0
	s_add_u32 s24, s18, 0x4900
	s_addc_u32 s25, s19, 0
	s_add_u32 s26, s18, 0x4a00
	s_addc_u32 s27, s19, 0
	s_add_u32 s28, s18, 0x4b00
	s_addc_u32 s29, s19, 0
	s_add_u32 s30, s18, 0x4c00
	s_addc_u32 s31, s19, 0
	s_add_u32 s48, s18, 0x4d00
	s_addc_u32 s49, s19, 0
	s_add_u32 s50, s18, 0x4e00
	s_addc_u32 s51, s19, 0
	s_add_u32 s52, s18, 0x4f00
	s_addc_u32 s53, s19, 0
	s_add_u32 s54, s18, 0x5000
	s_load_dwordx2 s[0:1], s[96:97], 0x4
	s_addc_u32 s55, s19, 0
	s_add_u32 s56, s18, 0x5100
	s_addc_u32 s57, s19, 0
	s_add_u32 s58, s18, 0x5200
	s_addc_u32 s59, s19, 0
	s_waitcnt lgkmcnt(0)
	s_mul_i32 s0, s0, s38
	s_add_u32 s60, s18, 0x5300
	s_mul_i32 s0, s0, s1
	s_addc_u32 s61, s19, 0
	s_mov_b32 s1, 1
	v_mov_b32_e32 v16, 0
	s_branch .LBB0_304
